# speedup vs baseline: 1.0106x; 1.0106x over previous
.LBB2_12:
	s_or_b32 s36, s1, s48
	v_readfirstlane_b32 s100, v160
	v_readfirstlane_b32 s101, v161
	v_and_b32_e32 v4, 0xfffff000, v181
	s_lshl_b32 s37, s36, 7
	s_add_u32 s100, s100, s76
	s_addc_u32 s101, s101, s77
	s_add_u32 s100, s100, s37
	s_addc_u32 s101, s101, 0
	v_readfirstlane_b32 s37, v4
	s_mov_b32 m0, s37
	s_nop 0
	global_load_lds_dwordx4 v172, s[100:101]
	global_load_lds_dwordx4 v174, s[100:101] offset:1024
	global_load_lds_dwordx4 v172, s[100:101] offset:2048
	global_load_lds_dwordx4 v174, s[100:101] offset:3072
	v_and_b32_e32 v5, 0xfff, v176
	v_add_u32_e32 v5, v5, v4
	v_writelane_b32 v252, s36, 37
	s_sub_i32 s36, s36, s33
	s_cmp_lt_i32 s36, 0
	s_waitcnt vmcnt(0) lgkmcnt(0)
	s_barrier
	v_add_u32_e32 v2, v5, v177
	v_add_u32_e32 v4, v5, v178
	ds_read_b128 v[122:125], v2
	ds_read_b128 v[126:129], v4
	v_add_u32_e32 v2, v5, v179
	v_add_u32_e32 v4, v5, v180
	ds_read_b128 v[130:133], v2
	ds_read_b128 v[134:137], v4
	s_cbranch_scc1 .LBB2_20
	s_lshl_b32 s36, s36, 7
	s_and_b32 s37, s36, 0x7000
	v_add_u32_e32 v2, s37, v176
	v_add_u32_e32 v4, v2, v177
	ds_read_b128 v[4:7], v4 offset:32768
	v_add_u32_e32 v8, v2, v178
	ds_read_b128 v[8:11], v8 offset:32768
	s_add_i32 s37, s36, 0x7000
	s_and_b32 s37, s37, 0x7000
	s_waitcnt lgkmcnt(1)
	v_mfma_f32_32x32x16_f16 v[20:35], v[122:125], v[4:7], 0
	v_add_u32_e32 v4, v2, v179
	ds_read_b128 v[4:7], v4 offset:32768
	v_add_u32_e32 v2, v2, v180
	s_addk_i32 s36, 0x6000
	s_and_b32 s36, s36, 0x7000
	v_add_u32_e32 v52, s36, v176
	v_add_u32_e32 v44, v52, v178
	s_waitcnt lgkmcnt(1)
	v_mfma_f32_32x32x16_f16 v[20:35], v[126:129], v[8:11], v[20:35]
	ds_read_b128 v[8:11], v2 offset:32768
	v_add_u32_e32 v2, s37, v176
	v_add_u32_e32 v40, v2, v178
	ds_read_b128 v[40:43], v40 offset:32768
	ds_read_b128 v[44:47], v44 offset:32768
	v_add_u32_e32 v48, v52, v179
	ds_read_b128 v[48:51], v48 offset:32768
	s_waitcnt lgkmcnt(4)
	v_mfma_f32_32x32x16_f16 v[20:35], v[130:133], v[4:7], v[20:35]
	v_add_u32_e32 v4, v2, v177
	ds_read_b128 v[4:7], v4 offset:32768
	s_waitcnt lgkmcnt(4)
	v_mfma_f32_32x32x16_f16 v[20:35], v[134:137], v[8:11], v[20:35]
	v_add_u32_e32 v8, v52, v177
	ds_read_b128 v[36:39], v8 offset:32768
	s_waitcnt lgkmcnt(1)
	v_mfma_f32_32x32x16_f16 v[4:19], v[122:125], v[4:7], 0
	v_mfma_f32_32x32x16_f16 v[4:19], v[126:129], v[40:43], v[4:19]
	v_add_u32_e32 v40, v2, v179
	ds_read_b128 v[40:43], v40 offset:32768
	v_add_u32_e32 v2, v2, v180
	s_waitcnt lgkmcnt(0)
	v_mfma_f32_32x32x16_f16 v[4:19], v[130:133], v[40:43], v[4:19]
	ds_read_b128 v[40:43], v2 offset:32768
	v_add_u32_e32 v2, v52, v180
	ds_read_b128 v[54:57], v2 offset:32768
	v_mfma_f32_32x32x16_f16 v[70:85], v[122:125], v[36:39], 0
	s_waitcnt lgkmcnt(1)
	v_mfma_f32_32x32x16_f16 v[4:19], v[134:137], v[40:43], v[4:19]
	v_mfma_f32_32x32x16_f16 v[70:85], v[126:129], v[44:47], v[70:85]
	s_nop 10
	v_cndmask_b32_e64 v2, v20, v4, s[52:53]
	ds_write_b32 v181, v2
	v_cndmask_b32_e64 v2, v21, v5, s[4:5]
	ds_write_b32 v181, v2 offset:128
	v_cndmask_b32_e64 v2, v22, v6, s[6:7]
	ds_write_b32 v181, v2 offset:256
	v_cndmask_b32_e64 v2, v23, v7, s[8:9]
	v_mfma_f32_32x32x16_f16 v[70:85], v[130:133], v[48:51], v[70:85]
	ds_write_b32 v181, v2 offset:384
	v_cndmask_b32_e64 v2, v24, v8, s[10:11]
	ds_write_b32 v181, v2 offset:1024
	v_cndmask_b32_e64 v2, v25, v9, s[12:13]
	ds_write_b32 v181, v2 offset:1152
	v_cndmask_b32_e64 v2, v26, v10, s[14:15]
	ds_write_b32 v181, v2 offset:1280
	v_cndmask_b32_e64 v2, v27, v11, s[16:17]
	ds_write_b32 v181, v2 offset:1408
	v_cndmask_b32_e64 v2, v28, v12, s[18:19]
	s_waitcnt lgkmcnt(8)
	v_mfma_f32_32x32x16_f16 v[70:85], v[134:137], v[54:57], v[70:85]
	ds_write_b32 v181, v2 offset:2048
	v_cndmask_b32_e64 v2, v29, v13, s[20:21]
	ds_write_b32 v181, v2 offset:2176
	v_cndmask_b32_e64 v2, v30, v14, s[22:23]
	ds_write_b32 v181, v2 offset:2304
	v_cndmask_b32_e64 v2, v31, v15, s[24:25]
	ds_write_b32 v181, v2 offset:2432
	v_cndmask_b32_e64 v2, v32, v16, s[26:27]
	ds_write_b32 v181, v2 offset:3072
	v_cndmask_b32_e64 v2, v33, v17, s[28:29]
	ds_write_b32 v181, v2 offset:3200
	v_cndmask_b32_e64 v2, v34, v18, s[30:31]
	ds_write_b32 v181, v2 offset:3328
	v_cndmask_b32_e64 v2, v35, v19, s[34:35]
	ds_write_b32 v181, v2 offset:3456
	v_cndmask_b32_e64 v2, v4, v70, s[52:53]
	ds_read_b32 v38, v214
	ds_read_b32 v39, v215
	ds_read_b32 v40, v216
	ds_read_b32 v41, v217
	ds_read_b32 v42, v218
	ds_read_b32 v43, v219
	ds_read_b32 v44, v220
	ds_read_b32 v45, v221
	ds_read_b32 v46, v222
	ds_read_b32 v47, v223
	ds_read_b32 v48, v224
	ds_read_b32 v49, v225
	ds_read_b32 v50, v226
	ds_read_b32 v51, v227
	ds_read_b32 v52, v228
	ds_read_b32 v53, v229
	ds_write_b32 v181, v2
	v_cndmask_b32_e64 v2, v5, v71, s[4:5]
	ds_write_b32 v181, v2 offset:128
	v_cndmask_b32_e64 v2, v6, v72, s[6:7]
	ds_write_b32 v181, v2 offset:256
	v_cndmask_b32_e64 v2, v7, v73, s[8:9]
	ds_write_b32 v181, v2 offset:384
	v_cndmask_b32_e64 v2, v8, v74, s[10:11]
	ds_write_b32 v181, v2 offset:1024
	v_cndmask_b32_e64 v2, v9, v75, s[12:13]
	ds_write_b32 v181, v2 offset:1152
	v_cndmask_b32_e64 v2, v10, v76, s[14:15]
	ds_write_b32 v181, v2 offset:1280
	v_cndmask_b32_e64 v2, v11, v77, s[16:17]
	ds_write_b32 v181, v2 offset:1408
	v_cndmask_b32_e64 v2, v12, v78, s[18:19]
	ds_write_b32 v181, v2 offset:2048
	v_cndmask_b32_e64 v2, v13, v79, s[20:21]
	ds_write_b32 v181, v2 offset:2176
	v_cndmask_b32_e64 v2, v14, v80, s[22:23]
	ds_write_b32 v181, v2 offset:2304
	v_cndmask_b32_e64 v2, v15, v81, s[24:25]
	ds_write_b32 v181, v2 offset:2432
	v_cndmask_b32_e64 v2, v16, v82, s[26:27]
	ds_write_b32 v181, v2 offset:3072
	v_cndmask_b32_e64 v2, v17, v83, s[28:29]
	ds_write_b32 v181, v2 offset:3200
	v_cndmask_b32_e64 v2, v18, v84, s[30:31]
	ds_write_b32 v181, v2 offset:3328
	v_cndmask_b32_e64 v2, v19, v85, s[34:35]
	ds_write_b32 v181, v2 offset:3456
	ds_read_b32 v54, v214
	ds_read_b32 v55, v215
	ds_read_b32 v56, v216
	ds_read_b32 v57, v217
	ds_read_b32 v58, v218
	ds_read_b32 v59, v219
	ds_read_b32 v60, v220
	ds_read_b32 v61, v221
	ds_read_b32 v62, v222
	ds_read_b32 v63, v223
	ds_read_b32 v64, v224
	ds_read_b32 v65, v225
	ds_read_b32 v66, v226
	ds_read_b32 v67, v227
	ds_read_b32 v68, v228
	ds_read_b32 v69, v229
	s_branch .LBB2_21

	.amdhsa_kernel _Z11attn_kernelPKDF16_S0_S0_S0_PDF16_
		.amdhsa_group_segment_fixed_size 163840
		.amdhsa_private_segment_fixed_size 0
		.amdhsa_kernarg_size 40
		.amdhsa_user_sgpr_count 2
		.amdhsa_user_sgpr_dispatch_ptr 0
		.amdhsa_user_sgpr_queue_ptr 0
		.amdhsa_user_sgpr_kernarg_segment_ptr 1
		.amdhsa_user_sgpr_dispatch_id 0
		.amdhsa_user_sgpr_kernarg_preload_length 0
		.amdhsa_user_sgpr_kernarg_preload_offset 0
		.amdhsa_user_sgpr_private_segment_size 0
		.amdhsa_uses_dynamic_stack 0
		.amdhsa_enable_private_segment 0
		.amdhsa_system_sgpr_workgroup_id_x 1
		.amdhsa_system_sgpr_workgroup_id_y 0
		.amdhsa_system_sgpr_workgroup_id_z 0
		.amdhsa_system_sgpr_workgroup_info 0
		.amdhsa_system_vgpr_workitem_id 0
		.amdhsa_next_free_vgpr 253
		.amdhsa_next_free_sgpr 102
		.amdhsa_accum_offset 256
		.amdhsa_reserve_vcc 1
		.amdhsa_float_round_mode_32 0
		.amdhsa_float_round_mode_16_64 0
		.amdhsa_float_denorm_mode_32 3
		.amdhsa_float_denorm_mode_16_64 3
		.amdhsa_dx10_clamp 1
		.amdhsa_ieee_mode 1
		.amdhsa_fp16_overflow 0
		.amdhsa_tg_split 0
		.amdhsa_exception_fp_ieee_invalid_op 0
		.amdhsa_exception_fp_denorm_src 0
		.amdhsa_exception_fp_ieee_div_zero 0
		.amdhsa_exception_fp_ieee_overflow 0
		.amdhsa_exception_fp_ieee_underflow 0
		.amdhsa_exception_fp_ieee_inexact 0
		.amdhsa_exception_int_div_zero 0
	.end_amdhsa_kernel
